# v049 + conversion slot (2 items per wave) in the 108 workgroups idle during the last unit round of the layer-0 in-projection (P2 tail)
# baseline (speedup 1.0000x reference)
; #define LAS __attribute__((address_space(3)))
; __device__ __forceinline__ int tidx() { int t = threadIdx.x; asm volatile("" : "+v"(t)); return t; }
; __device__ __forceinline__ void phase_cvt_moe(LAS unsigned char* lds, const CvtMoe a) {
;     const int tid_ = tidx(), wave = tid_ >> 6, lane = tid_ & 63;
;     LAS float* scr = (LAS float*)(lds + wave * CVT_SCR);
;     const int gw = blockIdx.x * 8 + wave, NGW = gridDim.x * 8;
;     constexpr int IG = (D / 64) * (FF / 64), ID = (FF / 64) * (D / 64);
;     for (int it = gw; it < 2 * NE * (2 * IG + ID); it += NGW) {
;         const int e = it / (2 * IG + ID); int r = it % (2 * IG + ID);
;         if (r < 2 * IG) { const int up = r / IG; r %= IG; const int nblk = FF / 64, kb = r / nblk, nb = r % nblk, n0 = nb * 64;
.LBB0_55:
	s_or_b64 exec, exec, s[4:5]
	s_add_u32 s4, s90, 0x30a13600
	s_addc_u32 s5, s91, 0
	v_writelane_b32 v250, s4, 6
	v_mov_b32_e32 v4, v0
	s_nop 0
	v_writelane_b32 v250, s5, 7
	s_add_u32 s4, s90, 0x46a13600
	s_addc_u32 s5, s91, 0
	v_writelane_b32 v250, s4, 8
	v_ashrrev_i32_e32 v2, 6, v4
	v_add_u32_e32 v5, s14, v2
	v_writelane_b32 v250, s5, 9
	s_mov_b32 s4, 0xd280
	v_cmp_gt_i32_e32 vcc, s4, v5
	s_and_saveexec_b64 s[4:5], vcc
	s_cbranch_execz .LBB0_62
	s_movk_i32 s6, 0x4100
	v_mul_lo_u32 v3, v2, s6
	v_add_u32_e32 v8, 0, v3
	v_lshlrev_b32_e32 v3, 2, v4
	v_bfe_u32 v6, v4, 4, 2
	v_and_b32_e32 v44, 60, v3
	v_bfe_u32 v7, v4, 3, 3
	v_lshlrev_b32_e32 v4, 3, v4
	v_lshl_add_u32 v20, v44, 2, v8
	v_mul_u32_u24_e32 v21, 0x104, v6
	v_and_b32_e32 v4, 56, v4
	v_mul_u32_u24_e32 v9, 0x104, v4
	v_lshlrev_b32_e32 v10, 2, v7
	v_lshlrev_b32_e32 v16, 2, v2
	v_add_u32_e32 v20, v20, v21
	v_mov_b32_e32 v3, 0
	v_add3_u32 v8, v8, v9, v10
	v_or_b32_e32 v9, 8, v7
	v_or_b32_e32 v10, 16, v7
	v_or_b32_e32 v11, 24, v7
	v_or_b32_e32 v12, 32, v7
	v_or_b32_e32 v13, 40, v7
	v_or_b32_e32 v14, 48, v7
	v_or_b32_e32 v15, 56, v7
	v_lshl_add_u32 v16, s2, 5, v16
	v_lshlrev_b32_e32 v17, 2, v1
	v_lshl_add_u32 v18, v2, 6, s3
	v_lshlrev_b32_e32 v19, 6, v1
	s_mov_b64 s[6:7], 0
	s_mov_b32 s3, 0x3e0f83e1
	s_movk_i32 s10, 0x57f
	s_mov_b32 s11, 0xb00000
	v_add_u32_e32 v21, 0x410, v20
	v_add_u32_e32 v22, 0x418, v20
	v_add_u32_e32 v23, 0x820, v20
	v_add_u32_e32 v24, 0x828, v20
	v_add_u32_e32 v25, 0xc30, v20
	v_add_u32_e32 v26, 0xc38, v20
	v_add_u32_e32 v27, 0x1040, v20
	v_add_u32_e32 v28, 0x1048, v20
	v_add_u32_e32 v29, 0x1450, v20
	v_add_u32_e32 v30, 0x1458, v20
	v_add_u32_e32 v31, 0x1860, v20
	v_add_u32_e32 v32, 0x1868, v20
	v_add_u32_e32 v33, 0x1c70, v20
	v_add_u32_e32 v34, 0x1c78, v20
	v_add_u32_e32 v35, 0x2080, v20
	v_add_u32_e32 v36, 0x2088, v20
	v_add_u32_e32 v37, 0x2490, v20
	v_add_u32_e32 v38, 0x2498, v20
	v_add_u32_e32 v39, 0x28a0, v20
	v_add_u32_e32 v40, 0x28a8, v20
	v_add_u32_e32 v41, 0x2cb0, v20
	v_add_u32_e32 v42, 0x2cb8, v20
	s_movk_i32 s12, 0xba3
	s_mov_b32 s13, 0xb000
	s_mov_b32 s14, 0x16000
	s_mov_b32 s15, 0x21000
	s_mov_b32 s16, 0x2c000
	s_mov_b32 s17, 0x37000
	s_mov_b32 s18, 0x42000
	s_mov_b32 s19, 0x4d000
	s_mov_b32 s20, 0x58000
	s_mov_b32 s21, 0x63000
	s_mov_b32 s22, 0x6e000
	s_mov_b32 s23, 0x79000
	s_mov_b32 s24, 0x84000
	s_mov_b32 s25, 0x8f000
	s_mov_b32 s26, 0x9a000
	s_mov_b32 s27, 0xa5000
	s_mov_b32 s28, 0xd27f
	v_lshlrev_b32_e32 v2, 2, v44
	v_add_u32_e32 v43, 0x30c0, v20
	v_add_u32_e32 v44, 0x30c8, v20
	v_add_u32_e32 v45, 0x34d0, v20
	v_add_u32_e32 v46, 0x34d8, v20
	v_mov_b32_e32 v47, 6
	v_mov_b32_e32 v48, 1
	v_mov_b32_e32 v49, 8
	v_mov_b32_e32 v50, 7
	s_branch .LBB0_58

; #define LAS __attribute__((address_space(3)))
; __device__ __forceinline__ int tidx() { int t = threadIdx.x; asm volatile("" : "+v"(t)); return t; }
; __device__ __forceinline__ void cvt_item(const float* W, int K, int N, bf16_t* WT, int drow0, int k0, int n0, LAS float* scr, int lane) {
;     f32x4 v[16];
;     const int lr = lane >> 4, lc4 = (lane & 15) * 4;
; #pragma unroll
;     for (int i = 0; i < 16; ++i) v[i] = __builtin_nontemporal_load((const f32x4*)(W + (size_t)(k0 + 4 * i + lr) * N + n0 + lc4));
; #pragma unroll
;     for (int i = 0; i < 16; ++i) { LAS float* d = scr + (4 * i + lr) * 65 + lc4; d[0] = v[i][0]; d[1] = v[i][1]; d[2] = v[i][2]; d[3] = v[i][3]; }
; __device__ __forceinline__ void phase_cvt_moe(LAS unsigned char* lds, const CvtMoe a) {
;     const int tid_ = tidx(), wave = tid_ >> 6, lane = tid_ & 63;
;     LAS float* scr = (LAS float*)(lds + wave * CVT_SCR);
;     const int gw = blockIdx.x * 8 + wave, NGW = gridDim.x * 8;
;     constexpr int IG = (D / 64) * (FF / 64), ID = (FF / 64) * (D / 64);
;     for (int it = gw; it < 2 * NE * (2 * IG + ID); it += NGW) {
;         const int e = it / (2 * IG + ID); int r = it % (2 * IG + ID);
;         if (r < 2 * IG) { const int up = r / IG; r %= IG; const int nblk = FF / 64, kb = r / nblk, nb = r % nblk, n0 = nb * 64;
;             cvt_item((up ? a.wu : a.wg) + (size_t)e * D * FF, D, FF, a.gu + (size_t)e * 2 * FF * D, (n0 / 128) * 256 + up * 128 + (n0 % 128), kb * 64, n0, scr, lane); }
;         else { r -= 2 * IG; const int nblk = D / 64, kb = r / nblk, nb = r % nblk; cvt_item(a.wd + (size_t)e * FF * D, FF, D, a.dn + (size_t)e * D * FF, nb * 64, kb * 64, nb * 64, scr, lane); }
.LBB0_223:
.Lcvp2_entry:
	s_sub_i32 s0, s94, 0x8c
	s_cmp_lt_u32 s0, 0x6c
	s_cbranch_scc0 .Lcvp2_exit
	v_readlane_b32 s12, v250, 26
	v_readlane_b32 s13, v250, 27
	s_nop 3
	s_sub_u32 s12, s12, 0xc0
	s_subb_u32 s13, s13, 0
	s_load_dwordx2 s[96:97], s[12:13], 0x90
	s_load_dwordx2 s[98:99], s[12:13], 0x98
	s_load_dwordx2 s[34:35], s[12:13], 0xa0
	s_lshl_b32 s0, s0, 3
	s_add_i32 s0, s0, 0xd280
	v_mov_b32_e32 v131, 0x360
	s_waitcnt lgkmcnt(0)
	s_add_u32 s4, s90, 0x30a13600
	s_addc_u32 s5, s91, 0
	v_writelane_b32 v250, s4, 6
	v_mov_b32_e32 v130, v0
	s_nop 0
	v_writelane_b32 v250, s5, 7
	s_add_u32 s4, s90, 0x46a13600
	s_addc_u32 s5, s91, 0
	v_writelane_b32 v250, s4, 8
	v_ashrrev_i32_e32 v2, 6, v130
	v_add_u32_e32 v5, s0, v2
	v_writelane_b32 v250, s5, 9
	s_mov_b32 s4, 0xd940
	v_cmp_gt_i32_e32 vcc, s4, v5
	s_and_saveexec_b64 s[4:5], vcc
	s_cbranch_execz .Lcvp2_62
	s_movk_i32 s48, 0x4100
	v_mul_lo_u32 v3, v2, s48
	v_add_u32_e32 v8, 0, v3
	v_lshlrev_b32_e32 v3, 2, v130
	v_bfe_u32 v6, v130, 4, 2
	v_and_b32_e32 v44, 60, v3
	v_bfe_u32 v7, v130, 3, 3
	v_lshlrev_b32_e32 v130, 3, v130
	v_lshl_add_u32 v20, v44, 2, v8
	v_mul_u32_u24_e32 v21, 0x104, v6
	v_and_b32_e32 v130, 56, v130
	v_mul_u32_u24_e32 v9, 0x104, v130
	v_lshlrev_b32_e32 v10, 2, v7
	v_lshlrev_b32_e32 v16, 2, v2
	v_add_u32_e32 v20, v20, v21
	v_mov_b32_e32 v3, 0
	v_add3_u32 v8, v8, v9, v10
	v_or_b32_e32 v9, 8, v7
	v_or_b32_e32 v10, 16, v7
	v_or_b32_e32 v11, 24, v7
	v_or_b32_e32 v12, 32, v7
	v_or_b32_e32 v13, 40, v7
	v_or_b32_e32 v14, 48, v7
	v_or_b32_e32 v15, 56, v7
	v_lshlrev_b32_e32 v16, 2, v5
	v_lshlrev_b32_e32 v17, 2, v131
	v_lshlrev_b32_e32 v18, 6, v5
	v_lshlrev_b32_e32 v19, 6, v131
	s_mov_b64 s[48:49], 0
	s_mov_b32 s13, 0x3e0f83e1
	s_movk_i32 s10, 0x57f
	s_mov_b32 s11, 0xb00000
	v_add_u32_e32 v21, 0x410, v20
	v_add_u32_e32 v22, 0x418, v20
	v_add_u32_e32 v23, 0x820, v20
	v_add_u32_e32 v24, 0x828, v20
	v_add_u32_e32 v25, 0xc30, v20
	v_add_u32_e32 v26, 0xc38, v20
	v_add_u32_e32 v27, 0x1040, v20
	v_add_u32_e32 v28, 0x1048, v20
	v_add_u32_e32 v29, 0x1450, v20
	v_add_u32_e32 v30, 0x1458, v20
	v_add_u32_e32 v31, 0x1860, v20
	v_add_u32_e32 v32, 0x1868, v20
	v_add_u32_e32 v33, 0x1c70, v20
	v_add_u32_e32 v34, 0x1c78, v20
	v_add_u32_e32 v35, 0x2080, v20
	v_add_u32_e32 v36, 0x2088, v20
	v_add_u32_e32 v37, 0x2490, v20
	v_add_u32_e32 v38, 0x2498, v20
	v_add_u32_e32 v39, 0x28a0, v20
	v_add_u32_e32 v40, 0x28a8, v20
	v_add_u32_e32 v41, 0x2cb0, v20
	v_add_u32_e32 v42, 0x2cb8, v20
	s_movk_i32 s64, 0xba3
	s_mov_b32 s65, 0xb000
	s_mov_b32 s66, 0x16000
	s_mov_b32 s67, 0x21000
	s_mov_b32 s1, 0x2c000
	s_mov_b32 s68, 0x37000
	s_mov_b32 s69, 0x42000
	s_mov_b32 s31, 0x4d000
	s_mov_b32 s32, 0x58000
	s_mov_b32 s37, 0x63000
	s_mov_b32 s70, 0x6e000
	s_mov_b32 s51, 0x79000
	s_mov_b32 s59, 0x84000
	s_mov_b32 s81, 0x8f000
	s_mov_b32 s92, 0x9a000
	s_mov_b32 s27, 0xa5000
	s_mov_b32 s71, 0xd93f
	v_lshlrev_b32_e32 v2, 2, v44
	v_add_u32_e32 v43, 0x30c0, v20
	v_add_u32_e32 v44, 0x30c8, v20
	v_add_u32_e32 v45, 0x34d0, v20
	v_add_u32_e32 v46, 0x34d8, v20
	v_mov_b32_e32 v47, 6
	v_mov_b32_e32 v132, 1
	v_mov_b32_e32 v133, 8
	v_mov_b32_e32 v134, 7
	s_branch .Lcvp2_58
.Lcvp2_57:
	s_or_b64 exec, exec, s[74:75]
	v_add_u32_e32 v5, v5, v131
	v_cmp_lt_i32_e32 vcc, s71, v5
	v_add_u32_e32 v16, v16, v17
	s_or_b64 s[48:49], vcc, s[48:49]
	v_add_u32_e32 v18, v18, v19
	s_andn2_b64 exec, exec, s[48:49]
	s_cbranch_execz .Lcvp2_62
.Lcvp2_58:
	v_mul_hi_i32 v135, v5, s13
	v_lshrrev_b32_e32 v136, 31, v135
	v_ashrrev_i32_e32 v135, 9, v135
	v_add_u32_e32 v135, v135, v136
	v_mul_i32_i24_e32 v137, 0x840, v135
	v_sub_u32_e32 v136, v5, v137
	v_cmp_lt_i32_e32 vcc, s10, v136
	s_and_saveexec_b64 s[74:75], vcc
	s_xor_b64 s[74:75], exec, s[74:75]
	s_cbranch_execz .Lcvp2_60
	v_lshlrev_b32_e32 v136, 6, v137
	v_sub_u32_e32 v118, v18, v136
	v_lshlrev_b32_e32 v136, 2, v137
	v_sub_u32_e32 v136, v16, v136
	v_and_b32_e32 v136, 0x7fffffc0, v136
	v_mov_b64_e32 v[138:139], s[34:35]
	v_and_b32_e32 v119, 0x3c0, v118
	v_add_u32_e32 v120, 0xffffea00, v136
	v_mad_i64_i32 v[138:139], s[72:73], v135, s11, v[138:139]
	v_or_b32_e32 v112, v120, v6
	v_lshlrev_b32_e32 v136, 2, v119
	v_mov_b32_e32 v137, v3
	v_lshl_add_u64 v[136:137], v[138:139], 0, v[136:137]
	v_mov_b32_e32 v113, v3
	v_or_b32_e32 v138, 4, v112
	v_mov_b32_e32 v139, v3
	v_or_b32_e32 v144, 8, v112
	v_mov_b32_e32 v145, v3
	v_or_b32_e32 v146, 12, v112
	v_mov_b32_e32 v147, v3
	v_or_b32_e32 v68, 16, v112
	v_mov_b32_e32 v69, v3
	v_or_b32_e32 v70, 20, v112
	v_mov_b32_e32 v71, v3
	v_or_b32_e32 v76, 24, v112
	v_mov_b32_e32 v77, v3
	v_or_b32_e32 v78, 28, v112
	v_mov_b32_e32 v79, v3
	v_or_b32_e32 v84, 32, v112
	v_mov_b32_e32 v85, v3
	v_or_b32_e32 v86, 36, v112
	v_mov_b32_e32 v87, v3
	v_or_b32_e32 v92, 40, v112
	v_mov_b32_e32 v93, v3
	v_or_b32_e32 v94, 44, v112
	v_mov_b32_e32 v95, v3
	v_or_b32_e32 v100, 48, v112
	v_mov_b32_e32 v101, v3
	v_or_b32_e32 v102, 52, v112
	v_mov_b32_e32 v103, v3
	v_or_b32_e32 v108, 56, v112
	v_mov_b32_e32 v109, v3
	v_lshl_add_u64 v[114:115], v[136:137], 0, v[2:3]
	v_lshlrev_b64 v[136:137], 12, v[112:113]
	v_lshlrev_b64 v[138:139], 12, v[138:139]
	v_lshlrev_b64 v[144:145], 12, v[144:145]
	v_lshlrev_b64 v[146:147], 12, v[146:147]
	v_lshlrev_b64 v[68:69], 12, v[68:69]
	v_lshlrev_b64 v[70:71], 12, v[70:71]
	v_lshlrev_b64 v[76:77], 12, v[76:77]
	v_lshlrev_b64 v[78:79], 12, v[78:79]
	v_lshlrev_b64 v[84:85], 12, v[84:85]
	v_lshlrev_b64 v[86:87], 12, v[86:87]
	v_lshlrev_b64 v[92:93], 12, v[92:93]
	v_lshlrev_b64 v[94:95], 12, v[94:95]
	v_lshlrev_b64 v[100:101], 12, v[100:101]
	v_lshlrev_b64 v[102:103], 12, v[102:103]
	v_lshlrev_b64 v[108:109], 12, v[108:109]
	v_lshl_add_u64 v[136:137], v[114:115], 0, v[136:137]
; #define LAS __attribute__((address_space(3)))
; __device__ __forceinline__ unsigned cvt_pk_bf16(float lo, float hi) { const f32x2 v = {lo, hi}; const bf16v2_t r = __builtin_convertvector(v, bf16v2_t); return __builtin_bit_cast(unsigned, r); }
; __device__ __forceinline__ void cvt_item(const float* W, int K, int N, bf16_t* WT, int drow0, int k0, int n0, LAS float* scr, int lane) {
;     ...
;     for (int i = 0; i < 16; ++i) v[i] = __builtin_nontemporal_load((const f32x4*)(W + (size_t)(k0 + 4 * i + lr) * N + n0 + lc4));
; #pragma unroll
;     for (int i = 0; i < 16; ++i) { LAS float* d = scr + (4 * i + lr) * 65 + lc4; d[0] = v[i][0]; d[1] = v[i][1]; d[2] = v[i][2]; d[3] = v[i][3]; }
;     asm volatile("s_waitcnt lgkmcnt(0)" ::: "memory");
;     const int c = lane & 7;
; #pragma unroll
;     for (int j = 0; j < 8; ++j) { const int n = (lane >> 3) + 8 * j; const LAS float* s = scr + (8 * c) * 65 + n;
;         u32x4 o; o.x = cvt_pk_bf16(s[0 * 65], s[1 * 65]); o.y = cvt_pk_bf16(s[2 * 65], s[3 * 65]); o.z = cvt_pk_bf16(s[4 * 65], s[5 * 65]); o.w = cvt_pk_bf16(s[6 * 65], s[7 * 65]);
;         __builtin_nontemporal_store(o, (u32x4*)(WT + ((size_t)((drow0 + n) >> 7) * (K >> 6) + (k0 >> 6)) * 8192 + ((drow0 + n) & 127) * 64 + 8 * c)); }
	v_lshl_add_u64 v[140:141], v[114:115], 0, v[138:139]
	v_lshl_add_u64 v[144:145], v[114:115], 0, v[144:145]
	v_lshl_add_u64 v[64:65], v[114:115], 0, v[146:147]
	v_lshl_add_u64 v[68:69], v[114:115], 0, v[68:69]
	v_lshl_add_u64 v[72:73], v[114:115], 0, v[70:71]
	v_lshl_add_u64 v[76:77], v[114:115], 0, v[76:77]
	v_lshl_add_u64 v[80:81], v[114:115], 0, v[78:79]
	v_lshl_add_u64 v[84:85], v[114:115], 0, v[84:85]
	v_lshl_add_u64 v[88:89], v[114:115], 0, v[86:87]
	v_lshl_add_u64 v[92:93], v[114:115], 0, v[92:93]
	v_lshl_add_u64 v[96:97], v[114:115], 0, v[94:95]
	v_lshl_add_u64 v[100:101], v[114:115], 0, v[100:101]
	v_lshl_add_u64 v[104:105], v[114:115], 0, v[102:103]
	v_lshl_add_u64 v[108:109], v[114:115], 0, v[108:109]
	v_or_b32_e32 v112, 60, v112
	global_load_dwordx4 v[136:139], v[136:137], off nt
	s_nop 0
	global_load_dwordx4 v[140:143], v[140:141], off nt
	s_nop 0
	global_load_dwordx4 v[144:147], v[144:145], off nt
	s_nop 0
	global_load_dwordx4 v[64:67], v[64:65], off nt
	s_nop 0
	global_load_dwordx4 v[68:71], v[68:69], off nt
	s_nop 0
	global_load_dwordx4 v[72:75], v[72:73], off nt
	s_nop 0
	global_load_dwordx4 v[76:79], v[76:77], off nt
	s_nop 0
	global_load_dwordx4 v[80:83], v[80:81], off nt
	s_nop 0
	global_load_dwordx4 v[84:87], v[84:85], off nt
	s_nop 0
	global_load_dwordx4 v[88:91], v[88:89], off nt
	s_nop 0
	global_load_dwordx4 v[92:95], v[92:93], off nt
	s_nop 0
	global_load_dwordx4 v[96:99], v[96:97], off nt
	s_nop 0
	global_load_dwordx4 v[100:103], v[100:101], off nt
	s_nop 0
	global_load_dwordx4 v[104:107], v[104:105], off nt
	v_lshlrev_b64 v[112:113], 12, v[112:113]
	global_load_dwordx4 v[108:111], v[108:109], off nt
	v_lshl_add_u64 v[112:113], v[114:115], 0, v[112:113]
	global_load_dwordx4 v[112:115], v[112:113], off nt
	v_mul_hi_i32_i24_e32 v117, 0x580000, v135
	v_mul_i32_i24_e32 v116, 0x580000, v135
	v_add_u32_e32 v135, 0x38e0, v20
	s_waitcnt vmcnt(15)
	ds_write2_b32 v20, v136, v137 offset1:1
	ds_write2_b32 v20, v138, v139 offset0:2 offset1:3
	s_waitcnt vmcnt(14)
	ds_write2_b32 v21, v140, v141 offset1:1
	ds_write2_b32 v22, v142, v143 offset1:1
	s_waitcnt vmcnt(13)
	ds_write2_b32 v23, v144, v145 offset1:1
	ds_write2_b32 v24, v146, v147 offset1:1
	s_waitcnt vmcnt(12)
	ds_write2_b32 v25, v64, v65 offset1:1
	ds_write2_b32 v26, v66, v67 offset1:1
	s_waitcnt vmcnt(11)
	ds_write2_b32 v27, v68, v69 offset1:1
	ds_write2_b32 v28, v70, v71 offset1:1
	s_waitcnt vmcnt(10)
	ds_write2_b32 v29, v72, v73 offset1:1
	ds_write2_b32 v30, v74, v75 offset1:1
	s_waitcnt vmcnt(9)
	ds_write2_b32 v31, v76, v77 offset1:1
	ds_write2_b32 v32, v78, v79 offset1:1
	s_waitcnt vmcnt(8)
	ds_write2_b32 v33, v80, v81 offset1:1
	ds_write2_b32 v34, v82, v83 offset1:1
	s_waitcnt vmcnt(7)
	ds_write2_b32 v35, v84, v85 offset1:1
	ds_write2_b32 v36, v86, v87 offset1:1
	s_waitcnt vmcnt(6)
	ds_write2_b32 v37, v88, v89 offset1:1
	ds_write2_b32 v38, v90, v91 offset1:1
	s_waitcnt vmcnt(5)
	ds_write2_b32 v39, v92, v93 offset1:1
	ds_write2_b32 v40, v94, v95 offset1:1
	s_waitcnt vmcnt(4)
	ds_write2_b32 v41, v96, v97 offset1:1
	ds_write2_b32 v42, v98, v99 offset1:1
	s_waitcnt vmcnt(3)
	ds_write2_b32 v43, v100, v101 offset1:1
	ds_write2_b32 v44, v102, v103 offset1:1
	s_waitcnt vmcnt(2)
	ds_write2_b32 v45, v104, v105 offset1:1
	ds_write2_b32 v46, v106, v107 offset1:1
	v_readlane_b32 s72, v250, 8
	s_waitcnt vmcnt(1)
	ds_write2_b32 v135, v108, v109 offset1:1
	v_add_u32_e32 v135, 0x38e8, v20
	ds_write2_b32 v135, v110, v111 offset1:1
	v_add_u32_e32 v135, 0x3cf0, v20
	s_waitcnt vmcnt(0)
	ds_write2_b32 v135, v112, v113 offset1:1
	v_add_u32_e32 v135, 0x3cf8, v20
	ds_write2_b32 v135, v114, v115 offset1:1
	s_waitcnt lgkmcnt(0)
	ds_read2_b32 v[140:141], v8 offset0:65 offset1:73
	ds_read2_b32 v[142:143], v8 offset1:8
	ds_read2_b32 v[144:145], v8 offset0:130 offset1:138
	ds_read2_b32 v[146:147], v8 offset0:195 offset1:203
	v_add_u32_e32 v135, 0x400, v8
	ds_read2_b32 v[64:65], v135 offset0:4 offset1:12
	ds_read2_b32 v[66:67], v135 offset0:69 offset1:77
	ds_read2_b32 v[68:69], v135 offset0:134 offset1:142
	ds_read2_b32 v[70:71], v135 offset0:199 offset1:207
	v_lshrrev_b32_e32 v72, 6, v120
	s_waitcnt lgkmcnt(6)
	v_cvt_pk_bf16_f32 v136, v142, v140
	v_bfe_u32 v142, v118, 7, 3
	v_readlane_b32 s73, v250, 9
	v_or_b32_e32 v140, v119, v7
	v_mad_u32_u24 v72, v142, 44, v72
	v_mov_b32_e32 v73, v3
	v_lshl_add_u64 v[116:117], s[72:73], 0, v[116:117]
	v_lshlrev_b64 v[72:73], 14, v[72:73]
	v_lshlrev_b32_e32 v140, 7, v140
	v_lshl_add_u64 v[72:73], v[116:117], 0, v[72:73]
	v_and_b32_e32 v74, 0x2380, v140
	v_mov_b32_e32 v75, v3
	v_lshl_add_u64 v[74:75], v[72:73], 0, v[74:75]
	v_lshlrev_b32_e32 v76, 1, v130
	v_mov_b32_e32 v77, v3
	v_or_b32_e32 v140, v119, v9
	s_waitcnt lgkmcnt(4)
	v_cvt_pk_bf16_f32 v137, v144, v146
	s_waitcnt lgkmcnt(2)
	v_cvt_pk_bf16_f32 v138, v64, v66
	s_waitcnt lgkmcnt(0)
	v_cvt_pk_bf16_f32 v139, v68, v70
	v_lshl_add_u64 v[74:75], v[74:75], 0, v[76:77]
	v_lshlrev_b32_e32 v140, 7, v140
	global_store_dwordx4 v[74:75], v[136:139], off nt
	v_and_b32_e32 v140, 0x2780, v140
	s_nop 0
	v_cvt_pk_bf16_f32 v136, v143, v141
	v_mov_b32_e32 v141, v3
	v_lshl_add_u64 v[140:141], v[72:73], 0, v[140:141]
	v_cvt_pk_bf16_f32 v137, v145, v147
	v_cvt_pk_bf16_f32 v138, v65, v67
	v_cvt_pk_bf16_f32 v139, v69, v71
	v_lshl_add_u64 v[140:141], v[140:141], 0, v[76:77]
	ds_read2_b32 v[142:143], v8 offset0:16 offset1:24
	ds_read2_b32 v[144:145], v8 offset0:81 offset1:89
	ds_read2_b32 v[146:147], v8 offset0:146 offset1:154
	ds_read2_b32 v[64:65], v8 offset0:211 offset1:219
	ds_read2_b32 v[66:67], v135 offset0:20 offset1:28
	ds_read2_b32 v[68:69], v135 offset0:85 offset1:93
	ds_read2_b32 v[70:71], v135 offset0:150 offset1:158
	ds_read2_b32 v[74:75], v135 offset0:215 offset1:223
	global_store_dwordx4 v[140:141], v[136:139], off nt
	v_or_b32_e32 v140, v119, v10
	v_lshlrev_b32_e32 v140, 7, v140
	v_and_b32_e32 v140, 0x2b80, v140
	v_mov_b32_e32 v141, v3
	v_lshl_add_u64 v[140:141], v[72:73], 0, v[140:141]
	s_waitcnt lgkmcnt(6)
; #define LAS __attribute__((address_space(3)))
; __device__ __forceinline__ unsigned cvt_pk_bf16(float lo, float hi) { const f32x2 v = {lo, hi}; const bf16v2_t r = __builtin_convertvector(v, bf16v2_t); return __builtin_bit_cast(unsigned, r); }
; __device__ __forceinline__ void cvt_item(const float* W, int K, int N, bf16_t* WT, int drow0, int k0, int n0, LAS float* scr, int lane) {
;     ...
;     for (int j = 0; j < 8; ++j) { const int n = (lane >> 3) + 8 * j; const LAS float* s = scr + (8 * c) * 65 + n;
;         u32x4 o; o.x = cvt_pk_bf16(s[0 * 65], s[1 * 65]); o.y = cvt_pk_bf16(s[2 * 65], s[3 * 65]); o.z = cvt_pk_bf16(s[4 * 65], s[5 * 65]); o.w = cvt_pk_bf16(s[6 * 65], s[7 * 65]);
;         __builtin_nontemporal_store(o, (u32x4*)(WT + ((size_t)((drow0 + n) >> 7) * (K >> 6) + (k0 >> 6)) * 8192 + ((drow0 + n) & 127) * 64 + 8 * c)); }
;     asm volatile("s_waitcnt lgkmcnt(0)" ::: "memory");
; }
; __device__ __forceinline__ void phase_cvt_moe(LAS unsigned char* lds, const CvtMoe a) {
;     ...
;         if (r < 2 * IG) { const int up = r / IG; r %= IG; const int nblk = FF / 64, kb = r / nblk, nb = r % nblk, n0 = nb * 64;
;             cvt_item((up ? a.wu : a.wg) + (size_t)e * D * FF, D, FF, a.gu + (size_t)e * 2 * FF * D, (n0 / 128) * 256 + up * 128 + (n0 % 128), kb * 64, n0, scr, lane); }
;         else { r -= 2 * IG; const int nblk = D / 64, kb = r / nblk, nb = r % nblk; cvt_item(a.wd + (size_t)e * FF * D, FF, D, a.dn + (size_t)e * D * FF, nb * 64, kb * 64, nb * 64, scr, lane); }
	v_cvt_pk_bf16_f32 v136, v142, v144
	s_waitcnt lgkmcnt(4)
	v_cvt_pk_bf16_f32 v137, v146, v64
	s_waitcnt lgkmcnt(2)
	v_cvt_pk_bf16_f32 v138, v66, v68
	s_waitcnt lgkmcnt(0)
	v_cvt_pk_bf16_f32 v139, v70, v74
	v_lshl_add_u64 v[140:141], v[140:141], 0, v[76:77]
	global_store_dwordx4 v[140:141], v[136:139], off nt
	v_or_b32_e32 v140, v119, v11
	v_lshlrev_b32_e32 v140, 7, v140
	v_and_b32_e32 v140, 0x2f80, v140
	v_mov_b32_e32 v141, v3
	v_lshl_add_u64 v[140:141], v[72:73], 0, v[140:141]
	v_cvt_pk_bf16_f32 v136, v143, v145
	v_cvt_pk_bf16_f32 v137, v147, v65
	v_cvt_pk_bf16_f32 v138, v67, v69
	v_cvt_pk_bf16_f32 v139, v71, v75
	v_lshl_add_u64 v[140:141], v[140:141], 0, v[76:77]
	ds_read2_b32 v[142:143], v8 offset0:32 offset1:40
	ds_read2_b32 v[144:145], v8 offset0:97 offset1:105
	ds_read2_b32 v[146:147], v8 offset0:162 offset1:170
	ds_read2_b32 v[64:65], v8 offset0:227 offset1:235
	ds_read2_b32 v[66:67], v135 offset0:36 offset1:44
	ds_read2_b32 v[68:69], v135 offset0:101 offset1:109
	ds_read2_b32 v[70:71], v135 offset0:166 offset1:174
	ds_read2_b32 v[74:75], v135 offset0:231 offset1:239
	global_store_dwordx4 v[140:141], v[136:139], off nt
	v_or_b32_e32 v140, v119, v12
	v_lshlrev_b32_e32 v140, 7, v140
	v_and_b32_e32 v140, 0x3380, v140
	v_mov_b32_e32 v141, v3
	v_lshl_add_u64 v[140:141], v[72:73], 0, v[140:141]
	s_waitcnt lgkmcnt(6)
	v_cvt_pk_bf16_f32 v136, v142, v144
	s_waitcnt lgkmcnt(4)
	v_cvt_pk_bf16_f32 v137, v146, v64
	s_waitcnt lgkmcnt(2)
	v_cvt_pk_bf16_f32 v138, v66, v68
	s_waitcnt lgkmcnt(0)
	v_cvt_pk_bf16_f32 v139, v70, v74
	v_lshl_add_u64 v[140:141], v[140:141], 0, v[76:77]
	global_store_dwordx4 v[140:141], v[136:139], off nt
	v_or_b32_e32 v140, v119, v13
	v_lshlrev_b32_e32 v140, 7, v140
	v_cvt_pk_bf16_f32 v136, v143, v145
	v_cvt_pk_bf16_f32 v137, v147, v65
	v_cvt_pk_bf16_f32 v138, v67, v69
	v_cvt_pk_bf16_f32 v139, v71, v75
	v_and_b32_e32 v140, 0x3780, v140
	v_mov_b32_e32 v141, v3
	ds_read2_b32 v[142:143], v8 offset0:48 offset1:56
	ds_read2_b32 v[144:145], v8 offset0:113 offset1:121
	ds_read2_b32 v[146:147], v8 offset0:178 offset1:186
	ds_read2_b32 v[64:65], v8 offset0:243 offset1:251
	ds_read2_b32 v[66:67], v135 offset0:52 offset1:60
	ds_read2_b32 v[68:69], v135 offset0:117 offset1:125
	ds_read2_b32 v[70:71], v135 offset0:182 offset1:190
	ds_read2_b32 v[74:75], v135 offset0:247 offset1:255
	v_lshl_add_u64 v[140:141], v[72:73], 0, v[140:141]
	v_or_b32_e32 v135, v119, v14
	v_lshl_add_u64 v[140:141], v[140:141], 0, v[76:77]
	v_lshlrev_b32_e32 v135, 7, v135
	global_store_dwordx4 v[140:141], v[136:139], off nt
	v_and_b32_e32 v140, 0x3b80, v135
	v_mov_b32_e32 v141, v3
	v_lshl_add_u64 v[140:141], v[72:73], 0, v[140:141]
	v_or_b32_e32 v135, v119, v15
	s_waitcnt lgkmcnt(6)
	v_cvt_pk_bf16_f32 v136, v142, v144
	s_waitcnt lgkmcnt(4)
	v_cvt_pk_bf16_f32 v137, v146, v64
	s_waitcnt lgkmcnt(2)
	v_cvt_pk_bf16_f32 v138, v66, v68
	s_waitcnt lgkmcnt(0)
	v_cvt_pk_bf16_f32 v139, v70, v74
	v_lshl_add_u64 v[140:141], v[140:141], 0, v[76:77]
	v_lshlrev_b32_e32 v135, 7, v135
	global_store_dwordx4 v[140:141], v[136:139], off nt
	v_and_b32_e32 v140, 0x3f80, v135
	v_mov_b32_e32 v141, v3
	v_lshl_add_u64 v[140:141], v[72:73], 0, v[140:141]
	v_cvt_pk_bf16_f32 v136, v143, v145
	v_cvt_pk_bf16_f32 v137, v147, v65
	v_cvt_pk_bf16_f32 v138, v67, v69
	v_cvt_pk_bf16_f32 v139, v71, v75
	v_lshl_add_u64 v[140:141], v[140:141], 0, v[76:77]
	global_store_dwordx4 v[140:141], v[136:139], off nt
	s_waitcnt lgkmcnt(0)
.Lcvp2_60:
	s_andn2_saveexec_b64 s[74:75], s[74:75]
	s_cbranch_execz .Lcvp2_57
	v_mul_i32_i24_e32 v137, 0xba3, v136
	v_lshrrev_b32_e32 v138, 31, v137
	v_ashrrev_i32_e32 v137, 21, v137
	v_add_u16_e32 v117, v137, v138
	v_mul_lo_u16_e32 v137, 0x2c0, v117
	v_sub_u16_e32 v137, v136, v137
	v_mul_i32_i24_sdwa v138, sext(v137), s64 dst_sel:DWORD dst_unused:UNUSED_PAD src0_sel:WORD_0 src1_sel:DWORD
	v_lshrrev_b32_e32 v139, 31, v138
	v_ashrrev_i32_e32 v138, 17, v138
	v_add_u16_e32 v138, v138, v139
	v_bfe_i32 v116, v138, 0, 16
	v_mul_lo_u16_e32 v138, 44, v138
	v_add_u32_e32 v136, 0x2bf, v136
	v_sub_u16_e32 v122, v137, v138
	v_mov_b32_e32 v137, s99
	v_mov_b32_e32 v138, s97
	v_cmp_gt_u32_e32 vcc, s10, v136
	v_mov_b32_e32 v136, s98
	v_lshlrev_b32_sdwa v118, v47, sext(v122) dst_sel:DWORD dst_unused:UNUSED_PAD src0_sel:DWORD src1_sel:WORD_0
	v_cndmask_b32_e32 v137, v137, v138, vcc
	v_mov_b32_e32 v138, s96
	v_cndmask_b32_e32 v136, v136, v138, vcc
	v_mad_i64_i32 v[136:137], s[72:73], v135, s11, v[136:137]
	v_lshl_or_b32 v138, v116, 6, v6
	v_ashrrev_i32_e32 v119, 31, v118
	v_lshl_add_u64 v[136:137], v[118:119], 2, v[136:137]
	v_mul_i32_i24_e32 v138, 0xb00, v138
	v_lshl_add_u64 v[136:137], v[136:137], 0, v[2:3]
	v_ashrrev_i32_e32 v139, 31, v138
	v_lshl_add_u64 v[112:113], v[138:139], 2, v[136:137]
	v_add_co_u32_e32 v140, vcc, s65, v112
	v_readlane_b32 s72, v250, 6
	s_nop 0
	v_addc_co_u32_e32 v141, vcc, 0, v113, vcc
	v_add_co_u32_e32 v144, vcc, s66, v112
	global_load_dwordx4 v[136:139], v[112:113], off nt
	s_nop 0
	global_load_dwordx4 v[140:143], v[140:141], off nt
	v_addc_co_u32_e32 v145, vcc, 0, v113, vcc
	v_add_co_u32_e32 v64, vcc, s67, v112
	v_readlane_b32 s73, v250, 7
	s_nop 0
	v_addc_co_u32_e32 v65, vcc, 0, v113, vcc
	v_add_co_u32_e32 v68, vcc, s1, v112
	global_load_dwordx4 v[144:147], v[144:145], off nt
	s_nop 0
	global_load_dwordx4 v[64:67], v[64:65], off nt
	v_addc_co_u32_e32 v69, vcc, 0, v113, vcc
	v_add_co_u32_e32 v72, vcc, s68, v112
	v_mov_b64_e32 v[120:121], s[72:73]
	s_nop 0
	v_addc_co_u32_e32 v73, vcc, 0, v113, vcc
	v_add_co_u32_e32 v76, vcc, s69, v112
	global_load_dwordx4 v[68:71], v[68:69], off nt
	s_nop 0
	global_load_dwordx4 v[72:75], v[72:73], off nt
	v_addc_co_u32_e32 v77, vcc, 0, v113, vcc
; #define LAS __attribute__((address_space(3)))
; __device__ __forceinline__ unsigned cvt_pk_bf16(float lo, float hi) { const f32x2 v = {lo, hi}; const bf16v2_t r = __builtin_convertvector(v, bf16v2_t); return __builtin_bit_cast(unsigned, r); }
; __device__ __forceinline__ void cvt_item(const float* W, int K, int N, bf16_t* WT, int drow0, int k0, int n0, LAS float* scr, int lane) {
;     ...
;     for (int i = 0; i < 16; ++i) v[i] = __builtin_nontemporal_load((const f32x4*)(W + (size_t)(k0 + 4 * i + lr) * N + n0 + lc4));
; #pragma unroll
;     for (int i = 0; i < 16; ++i) { LAS float* d = scr + (4 * i + lr) * 65 + lc4; d[0] = v[i][0]; d[1] = v[i][1]; d[2] = v[i][2]; d[3] = v[i][3]; }
;     asm volatile("s_waitcnt lgkmcnt(0)" ::: "memory");
;     const int c = lane & 7;
; #pragma unroll
;     for (int j = 0; j < 8; ++j) { const int n = (lane >> 3) + 8 * j; const LAS float* s = scr + (8 * c) * 65 + n;
;         u32x4 o; o.x = cvt_pk_bf16(s[0 * 65], s[1 * 65]); o.y = cvt_pk_bf16(s[2 * 65], s[3 * 65]); o.z = cvt_pk_bf16(s[4 * 65], s[5 * 65]); o.w = cvt_pk_bf16(s[6 * 65], s[7 * 65]);
;         __builtin_nontemporal_store(o, (u32x4*)(WT + ((size_t)((drow0 + n) >> 7) * (K >> 6) + (k0 >> 6)) * 8192 + ((drow0 + n) & 127) * 64 + 8 * c)); }
; __device__ __forceinline__ void phase_cvt_moe(LAS unsigned char* lds, const CvtMoe a) {
;     ...
;             cvt_item((up ? a.wu : a.wg) + (size_t)e * D * FF, D, FF, a.gu + (size_t)e * 2 * FF * D, (n0 / 128) * 256 + up * 128 + (n0 % 128), kb * 64, n0, scr, lane); }
	v_add_co_u32_e32 v80, vcc, s31, v112
	v_ashrrev_i16_e32 v119, 15, v118
	s_nop 0
	v_addc_co_u32_e32 v81, vcc, 0, v113, vcc
	v_add_co_u32_e32 v84, vcc, s32, v112
	global_load_dwordx4 v[76:79], v[76:77], off nt
	s_nop 0
	global_load_dwordx4 v[80:83], v[80:81], off nt
	v_addc_co_u32_e32 v85, vcc, 0, v113, vcc
	v_add_co_u32_e32 v88, vcc, s37, v112
	v_mad_i64_i32 v[120:121], s[72:73], v135, s11, v[120:121]
	s_nop 0
	v_addc_co_u32_e32 v89, vcc, 0, v113, vcc
	v_add_co_u32_e32 v92, vcc, s70, v112
	global_load_dwordx4 v[84:87], v[84:85], off nt
	s_nop 0
	global_load_dwordx4 v[88:91], v[88:89], off nt
	v_addc_co_u32_e32 v93, vcc, 0, v113, vcc
	v_add_co_u32_e32 v96, vcc, s51, v112
	v_lshrrev_b16_e32 v135, 7, v122
	s_nop 0
	v_addc_co_u32_e32 v97, vcc, 0, v113, vcc
	v_add_co_u32_e32 v100, vcc, s59, v112
	global_load_dwordx4 v[92:95], v[92:93], off nt
	s_nop 0
	global_load_dwordx4 v[96:99], v[96:97], off nt
	v_addc_co_u32_e32 v101, vcc, 0, v113, vcc
	v_add_co_u32_e32 v104, vcc, s81, v112
	v_lshrrev_b16_e32 v119, 9, v119
	s_nop 0
	v_addc_co_u32_e32 v105, vcc, 0, v113, vcc
	v_add_co_u32_e32 v108, vcc, s92, v112
	global_load_dwordx4 v[100:103], v[100:101], off nt
	s_nop 0
	global_load_dwordx4 v[104:107], v[104:105], off nt
	v_addc_co_u32_e32 v109, vcc, 0, v113, vcc
	global_load_dwordx4 v[108:111], v[108:109], off nt
	v_add_co_u32_e32 v112, vcc, s27, v112
	v_and_b32_e32 v135, 1, v135
	s_nop 0
	v_addc_co_u32_e32 v113, vcc, 0, v113, vcc
	global_load_dwordx4 v[112:115], v[112:113], off nt
	v_add_u16_e32 v119, v118, v119
	v_add_u16_e32 v135, v122, v135
	v_and_b32_e32 v119, 0xffffff80, v119
	v_ashrrev_i16_sdwa v135, v132, sext(v135) dst_sel:DWORD dst_unused:UNUSED_PAD src0_sel:DWORD src1_sel:BYTE_0
	v_sub_u16_e32 v118, v118, v119
	v_lshlrev_b32_sdwa v135, v133, sext(v135) dst_sel:DWORD dst_unused:UNUSED_PAD src0_sel:DWORD src1_sel:WORD_0
	v_lshlrev_b32_sdwa v117, v134, sext(v117) dst_sel:DWORD dst_unused:UNUSED_PAD src0_sel:DWORD src1_sel:WORD_0
	v_bfe_i32 v118, v118, 0, 16
	v_add3_u32 v135, v135, v117, v118
	v_ashrrev_i32_e32 v117, 31, v116
	s_waitcnt vmcnt(15)
	ds_write2_b32 v20, v136, v137 offset1:1
	ds_write2_b32 v20, v138, v139 offset0:2 offset1:3
	s_waitcnt vmcnt(14)
	ds_write2_b32 v21, v140, v141 offset1:1
	ds_write2_b32 v22, v142, v143 offset1:1
	s_waitcnt vmcnt(13)
	ds_write2_b32 v23, v144, v145 offset1:1
	ds_write2_b32 v24, v146, v147 offset1:1
	s_waitcnt vmcnt(12)
	ds_write2_b32 v25, v64, v65 offset1:1
	ds_write2_b32 v26, v66, v67 offset1:1
	s_waitcnt vmcnt(11)
	ds_write2_b32 v27, v68, v69 offset1:1
	ds_write2_b32 v28, v70, v71 offset1:1
	s_waitcnt vmcnt(10)
	ds_write2_b32 v29, v72, v73 offset1:1
	ds_write2_b32 v30, v74, v75 offset1:1
	s_waitcnt vmcnt(9)
	ds_write2_b32 v31, v76, v77 offset1:1
	ds_write2_b32 v32, v78, v79 offset1:1
	s_waitcnt vmcnt(8)
	ds_write2_b32 v33, v80, v81 offset1:1
	ds_write2_b32 v34, v82, v83 offset1:1
	s_waitcnt vmcnt(7)
	ds_write2_b32 v35, v84, v85 offset1:1
	ds_write2_b32 v36, v86, v87 offset1:1
	s_waitcnt vmcnt(6)
	ds_write2_b32 v37, v88, v89 offset1:1
	ds_write2_b32 v38, v90, v91 offset1:1
	s_waitcnt vmcnt(5)
	ds_write2_b32 v39, v92, v93 offset1:1
	ds_write2_b32 v40, v94, v95 offset1:1
	s_waitcnt vmcnt(4)
	ds_write2_b32 v41, v96, v97 offset1:1
	ds_write2_b32 v42, v98, v99 offset1:1
	s_waitcnt vmcnt(3)
	ds_write2_b32 v43, v100, v101 offset1:1
	ds_write2_b32 v44, v102, v103 offset1:1
	s_waitcnt vmcnt(2)
	ds_write2_b32 v45, v104, v105 offset1:1
	ds_write2_b32 v46, v106, v107 offset1:1
	v_add_u32_e32 v136, 0x38e0, v20
	v_add_u32_e32 v78, 0x400, v8
	s_waitcnt vmcnt(1)
	ds_write2_b32 v136, v108, v109 offset1:1
	v_add_u32_e32 v136, 0x38e8, v20
	ds_write2_b32 v136, v110, v111 offset1:1
	v_add_u32_e32 v136, 0x3cf0, v20
	v_ashrrev_i32_e32 v72, 7, v135
	v_ashrrev_i32_e32 v73, 31, v72
	s_waitcnt vmcnt(0)
	ds_write2_b32 v136, v112, v113 offset1:1
	v_add_u32_e32 v136, 0x3cf8, v20
	ds_write2_b32 v136, v114, v115 offset1:1
	s_waitcnt lgkmcnt(0)
	ds_read2_b32 v[140:141], v8 offset0:65 offset1:73
	ds_read2_b32 v[142:143], v8 offset1:8
	ds_read2_b32 v[144:145], v8 offset0:130 offset1:138
	ds_read2_b32 v[146:147], v8 offset0:195 offset1:203
	ds_read2_b32 v[64:65], v78 offset0:4 offset1:12
	ds_read2_b32 v[66:67], v78 offset0:69 offset1:77
	ds_read2_b32 v[68:69], v78 offset0:134 offset1:142
	ds_read2_b32 v[70:71], v78 offset0:199 offset1:207
	v_lshlrev_b64 v[72:73], 18, v[72:73]
	s_waitcnt lgkmcnt(6)
	v_cvt_pk_bf16_f32 v136, v142, v140
	v_or_b32_e32 v140, v135, v7
	v_lshlrev_b64 v[74:75], 14, v[116:117]
	v_lshl_add_u64 v[72:73], v[120:121], 0, v[72:73]
	v_lshlrev_b32_e32 v140, 7, v140
	v_lshl_add_u64 v[72:73], v[72:73], 0, v[74:75]
	v_and_b32_e32 v74, 0x3f80, v140
	v_mov_b32_e32 v75, v3
	v_lshl_add_u64 v[74:75], v[72:73], 0, v[74:75]
	v_lshlrev_b32_e32 v76, 1, v130
	v_mov_b32_e32 v77, v3
	v_or_b32_e32 v140, v135, v9
	s_waitcnt lgkmcnt(4)
	v_cvt_pk_bf16_f32 v137, v144, v146
	s_waitcnt lgkmcnt(2)
	v_cvt_pk_bf16_f32 v138, v64, v66
	s_waitcnt lgkmcnt(0)
; #define LAS __attribute__((address_space(3)))
; __device__ __forceinline__ unsigned cvt_pk_bf16(float lo, float hi) { const f32x2 v = {lo, hi}; const bf16v2_t r = __builtin_convertvector(v, bf16v2_t); return __builtin_bit_cast(unsigned, r); }
; __device__ __forceinline__ void cvt_item(const float* W, int K, int N, bf16_t* WT, int drow0, int k0, int n0, LAS float* scr, int lane) {
;     ...
;     for (int j = 0; j < 8; ++j) { const int n = (lane >> 3) + 8 * j; const LAS float* s = scr + (8 * c) * 65 + n;
;         u32x4 o; o.x = cvt_pk_bf16(s[0 * 65], s[1 * 65]); o.y = cvt_pk_bf16(s[2 * 65], s[3 * 65]); o.z = cvt_pk_bf16(s[4 * 65], s[5 * 65]); o.w = cvt_pk_bf16(s[6 * 65], s[7 * 65]);
;         __builtin_nontemporal_store(o, (u32x4*)(WT + ((size_t)((drow0 + n) >> 7) * (K >> 6) + (k0 >> 6)) * 8192 + ((drow0 + n) & 127) * 64 + 8 * c)); }
;     asm volatile("s_waitcnt lgkmcnt(0)" ::: "memory");
; }
; __device__ __forceinline__ void xcd_barrier(const XcdBarrier& b) {
;     asm volatile("s_waitcnt vmcnt(0)" ::: "memory");
;     __syncthreads();
;     if (threadIdx.x == 0) {
;         unsigned* bar = b.bar;
;         __builtin_amdgcn_s_waitcnt(0);
;         unsigned nloc = b.st[0], nx = b.st[1];
;         if (nloc == 0u) { xcd_barrier_complete(bar, b.x, nloc, nx); b.st[0] = nloc; b.st[1] = nx; }
	v_cvt_pk_bf16_f32 v139, v68, v70
	v_lshl_add_u64 v[74:75], v[74:75], 0, v[76:77]
	v_lshlrev_b32_e32 v140, 7, v140
	global_store_dwordx4 v[74:75], v[136:139], off nt
	v_and_b32_e32 v140, 0x3f80, v140
	s_nop 0
	v_cvt_pk_bf16_f32 v136, v143, v141
	v_mov_b32_e32 v141, v3
	v_lshl_add_u64 v[140:141], v[72:73], 0, v[140:141]
	v_cvt_pk_bf16_f32 v137, v145, v147
	v_cvt_pk_bf16_f32 v138, v65, v67
	v_cvt_pk_bf16_f32 v139, v69, v71
	v_lshl_add_u64 v[140:141], v[140:141], 0, v[76:77]
	ds_read2_b32 v[142:143], v8 offset0:16 offset1:24
	ds_read2_b32 v[144:145], v8 offset0:81 offset1:89
	ds_read2_b32 v[146:147], v8 offset0:146 offset1:154
	ds_read2_b32 v[64:65], v8 offset0:211 offset1:219
	ds_read2_b32 v[66:67], v78 offset0:20 offset1:28
	ds_read2_b32 v[68:69], v78 offset0:85 offset1:93
	ds_read2_b32 v[70:71], v78 offset0:150 offset1:158
	ds_read2_b32 v[74:75], v78 offset0:215 offset1:223
	global_store_dwordx4 v[140:141], v[136:139], off nt
	v_or_b32_e32 v140, v135, v10
	v_lshlrev_b32_e32 v140, 7, v140
	v_and_b32_e32 v140, 0x3f80, v140
	v_mov_b32_e32 v141, v3
	v_lshl_add_u64 v[140:141], v[72:73], 0, v[140:141]
	s_waitcnt lgkmcnt(6)
	v_cvt_pk_bf16_f32 v136, v142, v144
	s_waitcnt lgkmcnt(4)
	v_cvt_pk_bf16_f32 v137, v146, v64
	s_waitcnt lgkmcnt(2)
	v_cvt_pk_bf16_f32 v138, v66, v68
	s_waitcnt lgkmcnt(0)
	v_cvt_pk_bf16_f32 v139, v70, v74
	v_lshl_add_u64 v[140:141], v[140:141], 0, v[76:77]
	global_store_dwordx4 v[140:141], v[136:139], off nt
	v_or_b32_e32 v140, v135, v11
	v_lshlrev_b32_e32 v140, 7, v140
	v_and_b32_e32 v140, 0x3f80, v140
	v_mov_b32_e32 v141, v3
	v_lshl_add_u64 v[140:141], v[72:73], 0, v[140:141]
	v_cvt_pk_bf16_f32 v136, v143, v145
	v_cvt_pk_bf16_f32 v137, v147, v65
	v_cvt_pk_bf16_f32 v138, v67, v69
	v_cvt_pk_bf16_f32 v139, v71, v75
	v_lshl_add_u64 v[140:141], v[140:141], 0, v[76:77]
	ds_read2_b32 v[142:143], v8 offset0:32 offset1:40
	ds_read2_b32 v[144:145], v8 offset0:97 offset1:105
	ds_read2_b32 v[146:147], v8 offset0:162 offset1:170
	ds_read2_b32 v[64:65], v8 offset0:227 offset1:235
	ds_read2_b32 v[66:67], v78 offset0:36 offset1:44
	ds_read2_b32 v[68:69], v78 offset0:101 offset1:109
	ds_read2_b32 v[70:71], v78 offset0:166 offset1:174
	ds_read2_b32 v[74:75], v78 offset0:231 offset1:239
	global_store_dwordx4 v[140:141], v[136:139], off nt
	v_or_b32_e32 v140, v135, v12
	v_lshlrev_b32_e32 v140, 7, v140
	v_and_b32_e32 v140, 0x3f80, v140
	v_mov_b32_e32 v141, v3
	v_lshl_add_u64 v[140:141], v[72:73], 0, v[140:141]
	s_waitcnt lgkmcnt(6)
	v_cvt_pk_bf16_f32 v136, v142, v144
	s_waitcnt lgkmcnt(4)
	v_cvt_pk_bf16_f32 v137, v146, v64
	s_waitcnt lgkmcnt(2)
	v_cvt_pk_bf16_f32 v138, v66, v68
	s_waitcnt lgkmcnt(0)
	v_cvt_pk_bf16_f32 v139, v70, v74
	v_lshl_add_u64 v[140:141], v[140:141], 0, v[76:77]
	global_store_dwordx4 v[140:141], v[136:139], off nt
	v_or_b32_e32 v140, v135, v13
	v_lshlrev_b32_e32 v140, 7, v140
	v_and_b32_e32 v140, 0x3f80, v140
	v_mov_b32_e32 v141, v3
	v_lshl_add_u64 v[140:141], v[72:73], 0, v[140:141]
	v_cvt_pk_bf16_f32 v136, v143, v145
	v_cvt_pk_bf16_f32 v137, v147, v65
	v_cvt_pk_bf16_f32 v138, v67, v69
	v_cvt_pk_bf16_f32 v139, v71, v75
	v_lshl_add_u64 v[140:141], v[140:141], 0, v[76:77]
	ds_read2_b32 v[142:143], v8 offset0:48 offset1:56
	ds_read2_b32 v[144:145], v8 offset0:113 offset1:121
	ds_read2_b32 v[146:147], v8 offset0:178 offset1:186
	ds_read2_b32 v[64:65], v8 offset0:243 offset1:251
	ds_read2_b32 v[66:67], v78 offset0:52 offset1:60
	ds_read2_b32 v[68:69], v78 offset0:117 offset1:125
	ds_read2_b32 v[70:71], v78 offset0:182 offset1:190
	ds_read2_b32 v[74:75], v78 offset0:247 offset1:255
	global_store_dwordx4 v[140:141], v[136:139], off nt
	v_or_b32_e32 v140, v135, v14
	v_lshlrev_b32_e32 v140, 7, v140
	v_and_b32_e32 v140, 0x3f80, v140
	v_mov_b32_e32 v141, v3
	v_lshl_add_u64 v[140:141], v[72:73], 0, v[140:141]
	v_or_b32_e32 v135, v135, v15
	s_waitcnt lgkmcnt(6)
	v_cvt_pk_bf16_f32 v136, v142, v144
	s_waitcnt lgkmcnt(4)
	v_cvt_pk_bf16_f32 v137, v146, v64
	s_waitcnt lgkmcnt(2)
	v_cvt_pk_bf16_f32 v138, v66, v68
	s_waitcnt lgkmcnt(0)
	v_cvt_pk_bf16_f32 v139, v70, v74
	v_lshl_add_u64 v[140:141], v[140:141], 0, v[76:77]
	v_lshlrev_b32_e32 v135, 7, v135
	global_store_dwordx4 v[140:141], v[136:139], off nt
	v_and_b32_e32 v140, 0x3f80, v135
	v_mov_b32_e32 v141, v3
	v_lshl_add_u64 v[140:141], v[72:73], 0, v[140:141]
	v_cvt_pk_bf16_f32 v136, v143, v145
	v_cvt_pk_bf16_f32 v137, v147, v65
	v_cvt_pk_bf16_f32 v138, v67, v69
	v_cvt_pk_bf16_f32 v139, v71, v75
	v_lshl_add_u64 v[140:141], v[140:141], 0, v[76:77]
	global_store_dwordx4 v[140:141], v[136:139], off nt
	s_waitcnt lgkmcnt(0)
	s_branch .Lcvp2_57
.Lcvp2_62:
	s_or_b64 exec, exec, s[4:5]
	s_branch .Lcvp2_exit
.Lcvp2_exit:
	s_waitcnt vmcnt(0)
	s_waitcnt vmcnt(0)
	s_barrier
	s_mov_b64 s[0:1], exec
	v_readlane_b32 s4, v250, 0
	v_readlane_b32 s5, v250, 1
	s_and_b64 s[4:5], s[0:1], s[4:5]
	s_mov_b64 exec, s[4:5]
	s_cbranch_execz .LBB0_275
	s_add_i32 s4, 0, 0x25ff0
	v_mov_b32_e32 v1, s4
	s_waitcnt vmcnt(0) expcnt(0) lgkmcnt(0)
	ds_read_b32 v3, v1
	s_add_i32 s4, 0, 0x25ff4
	v_mov_b32_e32 v1, s4
	ds_read_b32 v1, v1
	s_waitcnt lgkmcnt(1)
	v_cmp_ne_u32_e32 vcc, 0, v3
	s_cbranch_vccnz .LBB0_239
	v_readlane_b32 s14, v250, 26
	v_readlane_b32 s15, v250, 27
	s_load_dword s12, s[14:15], 0x14
	s_load_dwordx2 s[4:5], s[14:15], 0x4
	s_mov_b32 s25, 1
	v_mov_b32_e32 v17, 0
	s_waitcnt lgkmcnt(0)
	s_lshr_b32 s14, s12, 16
	s_and_b32 s12, s12, 0xffff
	s_cmp_lg_u32 s12, 0
	s_cselect_b64 s[12:13], -1, 0
	s_cmp_lg_u64 s[12:13], 0
	s_addc_u32 s4, s4, 0
	s_cmp_lg_u32 s14, 0
	s_cselect_b64 s[12:13], -1, 0
	s_cmp_lg_u64 s[12:13], 0
	s_mul_i32 s24, s4, s33
	s_addc_u32 s4, s5, 0
	s_mul_i32 s24, s24, s4
	s_add_u32 s4, s90, 0x1000
	s_addc_u32 s5, s91, 0
	s_add_u32 s12, s90, 0x1100
	s_addc_u32 s13, s91, 0
	s_add_u32 s14, s90, 0x1200
	s_addc_u32 s15, s91, 0
	s_add_u32 s16, s90, 0x1300
	s_addc_u32 s17, s91, 0
	s_branch .LBB0_227
